# final norm phase: prefetched row loads marked nt (single-use stream written to a different buffer)
# speedup vs baseline: 1.0067x; 1.0011x over previous
; __device__ __forceinline__ void phase_final(const bf16* H, float* out, const float* gain, int gw, int NGW, int lane) {
;     ...
;     for (int m0 = gw * NR; m0 < NTOK; m0 += NGW * NR) { u32x4 v[NR][2];
; #pragma unroll
;         for (int r = 0; r < NR; ++r)
; #pragma unroll
;             for (int j = 0; j < 2; ++j) v[r][j] = ((const u32x4*)(H + (size_t)(m0 + r) * DM))[lane + 64 * j];
.LBB0_1264:
	s_mov_b64 s[0:1], s[66:67]
	s_load_dword s0, s[0:1], 0x138
	s_waitcnt lgkmcnt(0)
	s_cmp_lt_i32 s0, 46
	s_cbranch_scc0 .LBB0_1269
	s_mov_b64 s[0:1], s[66:67]
	s_load_dword s0, s[0:1], 0x13c
	s_waitcnt lgkmcnt(0)
	s_cmp_lt_i32 s0, 46
	s_cbranch_scc1 .LBB0_1269
	s_lshl_b32 s0, s68, 3
	v_mbcnt_lo_u32_b32 v0, -1, 0
	v_mbcnt_hi_u32_b32 v0, -1, v0
	s_add_i32 s0, s0, s69
	v_add_u32_e32 v0, s70, v0
	s_cmpk_gt_i32 s0, 0x3fff
	s_cbranch_scc1 .LBB0_1269
	s_load_dwordx4 s[8:11], s[66:67], 0x120
	s_load_dwordx2 s[2:3], s[66:67], 0x130
	s_waitcnt vmcnt(0)
	v_and_b32_e32 v20, 63, v0
	v_lshlrev_b32_e32 v16, 5, v20
	s_lshl_b32 s6, s65, 5
	s_waitcnt lgkmcnt(0)
	global_load_dwordx4 v[0:3], v16, s[8:9] offset:16
	global_load_dwordx4 v[4:7], v16, s[8:9]
	global_load_dwordx4 v[8:11], v16, s[8:9] offset:2064
	global_load_dwordx4 v[12:15], v16, s[8:9] offset:2048
	s_lshl_b32 s8, s0, 2
	s_ashr_i32 s9, s8, 31
	s_lshl_b64 s[0:1], s[8:9], 12
	s_add_u32 s0, s10, s0
	v_mov_b32_e32 v17, 0
	s_addc_u32 s1, s11, s1
	v_lshl_add_u64 v[18:19], s[0:1], 0, v[16:17]
	s_mov_b64 s[0:1], 0x3810
	s_ashr_i32 s7, s6, 31
	v_lshl_add_u64 v[32:33], v[18:19], 0, s[0:1]
	s_lshl_b64 s[10:11], s[6:7], 12
	s_lshl_b64 s[0:1], s[8:9], 11
	s_add_u32 s0, s2, s0
	v_lshlrev_b32_e32 v16, 4, v20
	s_addc_u32 s1, s3, s1
	v_lshl_add_u64 v[16:17], s[0:1], 0, v[16:17]
	s_mov_b64 s[0:1], 0x4d201c00
	v_lshl_add_u64 v[34:35], v[16:17], 0, s[0:1]
	s_mov_b32 s0, 0x358637bd
	s_lshl_b64 s[12:13], s[6:7], 11
	s_movk_i32 s7, 0xf000
	s_mov_b32 s14, 0x3a800000
	s_mov_b32 s9, 0x800000
	s_movk_i32 s15, 0xd000
	s_movk_i32 s16, 0xe000
	v_mov_b64_e32 v[36:37], s[0:1]
	v_add_co_u32_e32 v42, vcc, 0xfffff000, v34
	s_nop 1
	v_addc_co_u32_e32 v43, vcc, -1, v35, vcc
	global_load_dwordx4 v[140:143], v[34:35], off offset:-2048 nt
	global_load_dwordx4 v[144:147], v[34:35], off offset:-3072 nt
	global_load_dwordx4 v[148:151], v[34:35], off nt
	global_load_dwordx4 v[152:155], v[34:35], off offset:-1024 nt
	global_load_dwordx4 v[156:159], v[42:43], off offset:-2048 nt
	global_load_dwordx4 v[160:163], v[42:43], off offset:-3072 nt
	global_load_dwordx4 v[164:167], v[42:43], off offset:-1024 nt
	global_load_dwordx4 v[168:171], v[34:35], off offset:-4096 nt
	v_lshl_add_u64 v[34:35], v[34:35], 0, s[12:13]
	s_waitcnt vmcnt(0)
.LBB0_1268:
	v_mov_b64_e32 v[28:29], v[140:141]
	v_mov_b64_e32 v[30:31], v[142:143]
	v_mov_b64_e32 v[24:25], v[144:145]
	v_mov_b64_e32 v[26:27], v[146:147]
	v_mov_b64_e32 v[20:21], v[148:149]
	v_mov_b64_e32 v[22:23], v[150:151]
	v_mov_b64_e32 v[16:17], v[152:153]
	v_mov_b64_e32 v[18:19], v[154:155]
	v_mov_b64_e32 v[46:47], v[156:157]
	v_mov_b64_e32 v[48:49], v[158:159]
	v_mov_b64_e32 v[50:51], v[160:161]
	v_mov_b64_e32 v[52:53], v[162:163]
	v_mov_b64_e32 v[54:55], v[164:165]
	v_mov_b64_e32 v[56:57], v[166:167]
	v_mov_b64_e32 v[58:59], v[168:169]
	v_mov_b64_e32 v[60:61], v[170:171]
	v_add_co_u32_e64 v38, s[0:1], s15, v32
	s_add_i32 s8, s8, s6
	s_nop 0
	v_addc_co_u32_e64 v39, s[0:1], -1, v33, s[0:1]
	v_add_co_u32_e64 v40, s[0:1], s16, v32
	s_cmp_lt_i32 s8, 0x10000
	s_cbranch_scc0 .Lfin_noload
	v_add_co_u32_e32 v42, vcc, 0xfffff000, v34
	s_nop 1
	v_addc_co_u32_e32 v43, vcc, -1, v35, vcc
	global_load_dwordx4 v[140:143], v[34:35], off offset:-2048 nt
	global_load_dwordx4 v[144:147], v[34:35], off offset:-3072 nt
	global_load_dwordx4 v[148:151], v[34:35], off nt
	global_load_dwordx4 v[152:155], v[34:35], off offset:-1024 nt
	global_load_dwordx4 v[156:159], v[42:43], off offset:-2048 nt
	global_load_dwordx4 v[160:163], v[42:43], off offset:-3072 nt
	global_load_dwordx4 v[164:167], v[42:43], off offset:-1024 nt
	global_load_dwordx4 v[168:171], v[34:35], off offset:-4096 nt
	v_lshl_add_u64 v[34:35], v[34:35], 0, s[12:13]
